# baseline (speedup 1.0000x reference)
.LBB2_10:
	v_mov_b32_e32 v11, v0
	s_waitcnt lgkmcnt(0)
	s_barrier
	s_lshl_b32 s8, s18, 7
	v_add_u32_e32 v2, 0xffffff00, v11
	v_lshlrev_b32_e32 v3, 3, v11
	v_and_b32_e32 v3, 56, v3
	v_mov_b32_e32 v4, 0x11000
	v_lshrrev_b32_e32 v12, 3, v2
	v_ashrrev_i32_e32 v2, 3, v2
	s_movk_i32 s10, 0xffc0
	s_or_b32 s8, s8, s17
	v_lshl_or_b32 v10, v3, 1, v4
	v_bfi_b32 v7, s10, v2, v12
	s_movk_i32 s11, 0x90
	v_or_b32_e32 v6, s8, v3
	v_mad_u64_u32 v[2:3], s[8:9], v7, s11, v[10:11]
	ds_read_b128 v[2:5], v2 offset:18432
	v_lshlrev_b32_e32 v14, 1, v6
	v_lshl_add_u32 v13, v7, 8, v14
	v_lshrrev_b32_e32 v15, 3, v11
	v_ashrrev_i32_e32 v6, 3, v11
	s_waitcnt lgkmcnt(0)
	buffer_store_dwordx4 v[2:5], v13, s[4:7], 0 offen sc1
	v_bfi_b32 v16, s10, v6, v15
	v_mad_u64_u32 v[6:7], s[8:9], v16, s11, v[10:11]
	v_add_u32_e32 v2, 0x100, v11
	v_ashrrev_i32_e32 v2, 3, v2
	v_bfi_b32 v17, s10, v2, v12
	v_mad_u64_u32 v[2:3], s[8:9], v17, s11, v[10:11]
	v_add_u32_e32 v11, 0x200, v11
	v_ashrrev_i32_e32 v11, 3, v11
	ds_read_b128 v[6:9], v6 offset:18432
	v_bfi_b32 v15, s10, v11, v15
	ds_read_b128 v[2:5], v2 offset:18432
	v_mad_u64_u32 v[10:11], s[8:9], v15, s11, v[10:11]
	ds_read_b128 v[10:13], v10 offset:18432
	v_lshl_add_u32 v16, v16, 8, v14
	s_waitcnt lgkmcnt(2)
	buffer_store_dwordx4 v[6:9], v16, s[4:7], 0 offen sc1
	s_nop 1
	v_lshl_add_u32 v6, v17, 8, v14
	s_waitcnt lgkmcnt(1)
	buffer_store_dwordx4 v[2:5], v6, s[4:7], 0 offen sc1
	s_nop 1
	v_lshl_add_u32 v2, v15, 8, v14
	s_waitcnt lgkmcnt(0)
	buffer_store_dwordx4 v[10:13], v2, s[4:7], 0 offen sc1
	s_mov_b64 s[2:3], 0

.LBB3_10:
	v_mov_b32_e32 v11, v0
	s_waitcnt lgkmcnt(0)
	s_barrier
	s_lshl_b32 s8, s19, 7
	v_add_u32_e32 v2, 0xffffff00, v11
	v_lshlrev_b32_e32 v3, 3, v11
	v_and_b32_e32 v3, 56, v3
	v_mov_b32_e32 v4, 0x11000
	v_lshrrev_b32_e32 v12, 3, v2
	v_ashrrev_i32_e32 v2, 3, v2
	s_movk_i32 s10, 0xffc0
	s_or_b32 s8, s8, s18
	v_lshl_or_b32 v10, v3, 1, v4
	v_bfi_b32 v7, s10, v2, v12
	s_movk_i32 s11, 0x90
	v_or_b32_e32 v6, s8, v3
	v_mad_u64_u32 v[2:3], s[8:9], v7, s11, v[10:11]
	ds_read_b128 v[2:5], v2 offset:18432
	v_lshlrev_b32_e32 v14, 1, v6
	v_lshl_add_u32 v13, v7, 8, v14
	v_lshrrev_b32_e32 v15, 3, v11
	v_ashrrev_i32_e32 v6, 3, v11
	s_waitcnt lgkmcnt(0)
	buffer_store_dwordx4 v[2:5], v13, s[4:7], 0 offen sc1
	v_bfi_b32 v16, s10, v6, v15
	v_mad_u64_u32 v[6:7], s[8:9], v16, s11, v[10:11]
	v_add_u32_e32 v2, 0x100, v11
	v_ashrrev_i32_e32 v2, 3, v2
	v_bfi_b32 v17, s10, v2, v12
	v_mad_u64_u32 v[2:3], s[8:9], v17, s11, v[10:11]
	v_add_u32_e32 v11, 0x200, v11
	v_ashrrev_i32_e32 v11, 3, v11
	ds_read_b128 v[6:9], v6 offset:18432
	v_bfi_b32 v15, s10, v11, v15
	ds_read_b128 v[2:5], v2 offset:18432
	v_mad_u64_u32 v[10:11], s[8:9], v15, s11, v[10:11]
	ds_read_b128 v[10:13], v10 offset:18432
	v_lshl_add_u32 v16, v16, 8, v14
	s_waitcnt lgkmcnt(2)
	buffer_store_dwordx4 v[6:9], v16, s[4:7], 0 offen sc1
	s_nop 1
	v_lshl_add_u32 v6, v17, 8, v14
	s_waitcnt lgkmcnt(1)
	buffer_store_dwordx4 v[2:5], v6, s[4:7], 0 offen sc1
	s_nop 1
	v_lshl_add_u32 v2, v15, 8, v14
	s_waitcnt lgkmcnt(0)
	buffer_store_dwordx4 v[10:13], v2, s[4:7], 0 offen sc1
	s_mov_b64 s[2:3], 0
